# MLA: deferred exp2 moved from QK^T gaps 1/2 to gaps 4/5 (no transcendental in the first cycles after the step barrier)
# speedup vs baseline: 1.0039x; 1.0039x over previous
.LBB0_1149:
	ds_read_b128 v[84:87], v156
	ds_read_b128 v[190:193], v156 offset:512
	ds_read_b128 v[194:197], v156 offset:2048
	ds_read_b128 v[198:201], v156 offset:2560
	s_setprio 1
	s_waitcnt lgkmcnt(0)
	v_mfma_f32_32x32x16_bf16 v[100:115], v[84:87], v[136:139], v[36:51]
	s_add_i32 s19, s27, -1
	s_and_b32 s18, s19, 3
	s_mul_i32 s20, s18, 0x3000
	s_and_b32 s17, s14, 0x6000
	v_add_f32_e32 v88, v68, v69
	ds_read_b128 v[202:205], v156 offset:4096
	ds_read_b64_tr_b16 v[172:173], v157 offset:49152
	ds_read_b64_tr_b16 v[174:175], v157 offset:49664
	v_add_f32_e32 v84, v70, v88
	v_add_f32_e32 v84, v71, v84
	v_add_f32_e32 v84, v72, v84
	v_add_f32_e32 v144, v73, v84
	v_cvt_pk_bf16_f32 v140, v68, v69
	v_cvt_pk_bf16_f32 v141, v70, v71
	v_mfma_f32_32x32x16_bf16 v[84:99], v[190:193], v[136:139], v[36:51]
	ds_read_b128 v[190:193], v156 offset:4608
	ds_read_b64_tr_b16 v[68:69], v157 offset:53248
	ds_read_b64_tr_b16 v[70:71], v157 offset:53760
	v_add_f32_e32 v142, v74, v144
	v_add_f32_e32 v142, v75, v142
	v_add_f32_e32 v142, v76, v142
	v_add_f32_e32 v144, v77, v142
	v_cvt_pk_bf16_f32 v142, v72, v73
	v_cvt_pk_bf16_f32 v143, v74, v75
	v_mfma_f32_32x32x16_bf16 v[100:115], v[194:197], v[132:135], v[100:115]
	ds_read_b128 v[194:197], v156 offset:6144
	ds_read_b64_tr_b16 v[72:73], v157 offset:50176
	ds_read_b64_tr_b16 v[74:75], v157 offset:50688
	v_add_f32_e32 v144, v78, v144
	v_add_f32_e32 v144, v79, v144
	v_add_f32_e32 v144, v80, v144
	v_add_f32_e32 v148, v81, v144
	v_cvt_pk_bf16_f32 v144, v76, v77
	v_cvt_pk_bf16_f32 v145, v78, v79
	v_mfma_f32_32x32x16_bf16 v[84:99], v[198:201], v[132:135], v[84:99]
	ds_read_b128 v[198:201], v156 offset:6656
	ds_read_b64_tr_b16 v[76:77], v157 offset:54272
	ds_read_b64_tr_b16 v[78:79], v157 offset:54784
	v_add_f32_e32 v146, v82, v148
	v_add_f32_e32 v146, v83, v146
	v_add_f32_e32 v146, v52, v146
	v_add_f32_e32 v148, v53, v146
	v_cvt_pk_bf16_f32 v146, v80, v81
	v_cvt_pk_bf16_f32 v147, v82, v83
	v_exp_f32_e32 v60, v60
	v_exp_f32_e32 v61, v61
	v_exp_f32_e32 v62, v62
	v_exp_f32_e32 v63, v63
	s_waitcnt lgkmcnt(0)
	v_mfma_f32_32x32x16_bf16 v[100:115], v[202:205], v[128:131], v[100:115]
	ds_read_b128 v[202:205], v156 offset:8192
	ds_read_b64_tr_b16 v[80:81], v157 offset:51200
	ds_read_b64_tr_b16 v[82:83], v157 offset:51712
	v_add_f32_e32 v148, v54, v148
	v_add_f32_e32 v148, v55, v148
	v_add_f32_e32 v148, v56, v148
	v_add_f32_e32 v152, v57, v148
	v_cvt_pk_bf16_f32 v148, v52, v53
	v_cvt_pk_bf16_f32 v149, v54, v55
	v_exp_f32_e32 v64, v64
	v_exp_f32_e32 v65, v65
	v_exp_f32_e32 v66, v66
	v_exp_f32_e32 v67, v67
	v_mfma_f32_32x32x16_bf16 v[84:99], v[190:193], v[128:131], v[84:99]
	ds_read_b128 v[190:193], v156 offset:8704
	ds_read_b64_tr_b16 v[52:53], v157 offset:55296
	ds_read_b64_tr_b16 v[54:55], v157 offset:55808
	v_add_f32_e32 v150, v58, v152
	v_add_f32_e32 v150, v59, v150
	v_add_f32_e32 v150, v60, v150
	v_add_f32_e32 v152, v61, v150
	v_cvt_pk_bf16_f32 v150, v56, v57
	v_cvt_pk_bf16_f32 v151, v58, v59
	v_mfma_f32_32x32x16_bf16 v[100:115], v[194:197], v[124:127], v[100:115]
	ds_read_b128 v[194:197], v156 offset:10240
	ds_read_b64_tr_b16 v[56:57], v157 offset:52224
	ds_read_b64_tr_b16 v[58:59], v157 offset:52736
	v_add_f32_e32 v152, v62, v152
	v_add_f32_e32 v152, v63, v152
	v_add_f32_e32 v152, v64, v152
	v_add_f32_e32 v160, v65, v152
	v_cvt_pk_bf16_f32 v152, v60, v61
	v_cvt_pk_bf16_f32 v153, v62, v63
	v_mfma_f32_32x32x16_bf16 v[84:99], v[198:201], v[124:127], v[84:99]
	ds_read_b128 v[198:201], v156 offset:10752
	ds_read_b64_tr_b16 v[60:61], v157 offset:56320
	ds_read_b64_tr_b16 v[62:63], v157 offset:56832
	v_add_f32_e32 v154, v66, v160
	v_add_f32_e32 v156, v67, v154
	v_cvt_pk_bf16_f32 v154, v64, v65
	v_cvt_pk_bf16_f32 v155, v66, v67
	s_waitcnt lgkmcnt(0)
	v_mfma_f32_32x32x16_bf16 v[100:115], v[202:205], v[120:123], v[100:115]
	s_add_i32 s16, s27, 2
	s_min_i32 s8, s16, s2
	s_lshl_b64 s[10:11], s[8:9], 17
	v_lshl_add_u64 v[202:203], v[176:177], 0, s[10:11]
	s_and_b32 s10, s16, 3
	s_mulk_i32 s10, 0x3000
	s_add_i32 s10, s26, s10
	s_mov_b32 m0, s10
	s_nop 0
	global_load_lds_dwordx4 v[202:203], off
	v_mfma_f32_32x32x16_bf16 v[84:99], v[190:193], v[120:123], v[84:99]
	s_and_b64 vcc, exec, s[38:39]
	s_cbranch_vccnz .Lmla_rope1
	s_lshl_b64 s[12:13], s[8:9], 18
	v_lshl_add_u64 v[202:203], v[180:181], 0, s[12:13]
	s_add_i32 m0, s10, 0x2000
	s_nop 0
	global_load_lds_dwordx4 v[202:203], off

.LBB0_1159:
	ds_read_b128 v[52:55], v140
	ds_read_b128 v[190:193], v140 offset:512
	ds_read_b128 v[194:197], v140 offset:2048
	ds_read_b128 v[198:201], v140 offset:2560
	s_setprio 1
	s_waitcnt lgkmcnt(0)
	v_mfma_f32_32x32x16_bf16 v[68:83], v[52:55], v[136:139], v[36:51]
	v_add_f32_e32 v56, v100, v101
	ds_read_b128 v[202:205], v140 offset:4096
	ds_read_b64_tr_b16 v[172:173], v141 offset:49152
	ds_read_b64_tr_b16 v[174:175], v141 offset:49664
	v_add_f32_e32 v52, v102, v56
	v_add_f32_e32 v52, v103, v52
	v_add_f32_e32 v52, v104, v52
	v_add_f32_e32 v144, v105, v52
	v_cvt_pk_bf16_f32 v156, v100, v101
	v_cvt_pk_bf16_f32 v157, v102, v103
	v_mfma_f32_32x32x16_bf16 v[52:67], v[190:193], v[136:139], v[36:51]
	ds_read_b128 v[190:193], v140 offset:4608
	ds_read_b64_tr_b16 v[100:101], v141 offset:53248
	ds_read_b64_tr_b16 v[102:103], v141 offset:53760
	v_add_f32_e32 v144, v106, v144
	v_add_f32_e32 v144, v107, v144
	v_add_f32_e32 v144, v108, v144
	v_add_f32_e32 v144, v109, v144
	v_cvt_pk_bf16_f32 v158, v104, v105
	v_cvt_pk_bf16_f32 v159, v106, v107
	v_mfma_f32_32x32x16_bf16 v[68:83], v[194:197], v[132:135], v[68:83]
	ds_read_b128 v[194:197], v140 offset:6144
	ds_read_b64_tr_b16 v[104:105], v141 offset:50176
	ds_read_b64_tr_b16 v[106:107], v141 offset:50688
	v_add_f32_e32 v144, v110, v144
	v_add_f32_e32 v144, v111, v144
	v_add_f32_e32 v144, v112, v144
	v_add_f32_e32 v144, v113, v144
	v_cvt_pk_bf16_f32 v160, v108, v109
	v_cvt_pk_bf16_f32 v161, v110, v111
	v_mfma_f32_32x32x16_bf16 v[52:67], v[198:201], v[132:135], v[52:67]
	ds_read_b128 v[198:201], v140 offset:6656
	ds_read_b64_tr_b16 v[108:109], v141 offset:54272
	ds_read_b64_tr_b16 v[110:111], v141 offset:54784
	v_add_f32_e32 v144, v114, v144
	v_add_f32_e32 v144, v115, v144
	v_add_f32_e32 v144, v84, v144
	v_add_f32_e32 v144, v85, v144
	v_cvt_pk_bf16_f32 v162, v112, v113
	v_cvt_pk_bf16_f32 v163, v114, v115
	v_exp_f32_e32 v92, v92
	v_exp_f32_e32 v93, v93
	v_exp_f32_e32 v94, v94
	v_exp_f32_e32 v95, v95
	s_waitcnt lgkmcnt(0)
	v_mfma_f32_32x32x16_bf16 v[68:83], v[202:205], v[128:131], v[68:83]
	ds_read_b128 v[202:205], v140 offset:8192
	ds_read_b64_tr_b16 v[112:113], v141 offset:51200
	ds_read_b64_tr_b16 v[114:115], v141 offset:51712
	v_add_f32_e32 v144, v86, v144
	v_add_f32_e32 v144, v87, v144
	v_add_f32_e32 v144, v88, v144
	v_add_f32_e32 v144, v89, v144
	v_cvt_pk_bf16_f32 v164, v84, v85
	v_cvt_pk_bf16_f32 v165, v86, v87
	v_exp_f32_e32 v96, v96
	v_exp_f32_e32 v97, v97
	v_exp_f32_e32 v98, v98
	v_exp_f32_e32 v99, v99
	v_mfma_f32_32x32x16_bf16 v[52:67], v[190:193], v[128:131], v[52:67]
	ds_read_b128 v[190:193], v140 offset:8704
	ds_read_b64_tr_b16 v[84:85], v141 offset:55296
	ds_read_b64_tr_b16 v[86:87], v141 offset:55808
	v_add_f32_e32 v144, v90, v144
	v_add_f32_e32 v144, v91, v144
	v_add_f32_e32 v144, v92, v144
	v_add_f32_e32 v144, v93, v144
	v_cvt_pk_bf16_f32 v166, v88, v89
	v_cvt_pk_bf16_f32 v167, v90, v91
	v_mfma_f32_32x32x16_bf16 v[68:83], v[194:197], v[124:127], v[68:83]
	ds_read_b128 v[194:197], v140 offset:10240
	ds_read_b64_tr_b16 v[88:89], v141 offset:52224
	ds_read_b64_tr_b16 v[90:91], v141 offset:52736
	v_add_f32_e32 v144, v94, v144
	v_add_f32_e32 v144, v95, v144
	v_add_f32_e32 v144, v96, v144
	v_add_f32_e32 v144, v97, v144
	v_cvt_pk_bf16_f32 v168, v92, v93
	v_cvt_pk_bf16_f32 v169, v94, v95
	v_mfma_f32_32x32x16_bf16 v[52:67], v[198:201], v[124:127], v[52:67]
	ds_read_b128 v[198:201], v140 offset:10752
	ds_read_b64_tr_b16 v[92:93], v141 offset:56320
	ds_read_b64_tr_b16 v[94:95], v141 offset:56832
	v_add_f32_e32 v140, v98, v144
	v_add_f32_e32 v140, v99, v140
	v_cvt_pk_bf16_f32 v170, v96, v97
	v_cvt_pk_bf16_f32 v171, v98, v99
	s_waitcnt lgkmcnt(0)
	v_mfma_f32_32x32x16_bf16 v[68:83], v[202:205], v[120:123], v[68:83]
	s_add_i32 s8, s27, 3
	s_min_i32 s8, s8, s2
	s_lshl_b64 s[10:11], s[8:9], 17
	v_lshl_add_u64 v[202:203], v[176:177], 0, s[10:11]
	s_add_i32 s10, s26, s20
	s_mov_b32 m0, s10
	s_nop 0
	global_load_lds_dwordx4 v[202:203], off
	v_mfma_f32_32x32x16_bf16 v[52:67], v[190:193], v[120:123], v[52:67]
	s_and_b64 vcc, exec, s[38:39]
	s_cbranch_vccnz .Lmla_rope2
	s_lshl_b64 s[12:13], s[8:9], 18
	v_lshl_add_u64 v[202:203], v[180:181], 0, s[12:13]
	s_add_i32 m0, s10, 0x2000
	s_nop 0
	global_load_lds_dwordx4 v[202:203], off

.LBB0_1181:
	s_xor_b32 s2, s15, 0x4000
	s_add_i32 s2, s2, 0
	v_lshl_add_u64 v[84:85], v[178:179], 0, s[8:9]
	s_add_i32 s2, s2, s34
	v_lshl_add_u64 v[84:85], v[84:85], 0, s[24:25]
	s_add_i32 m0, s2, 0xc000
	s_and_b32 s2, s12, 3
	global_load_lds_dwordx4 v[84:85], off
	s_mulk_i32 s2, 0x3000
	s_and_b32 s2, s14, 0x6000
	s_setprio 1
	s_waitcnt lgkmcnt(0)
	v_mfma_f32_32x32x16_bf16 v[84:99], v[100:103], v[136:139], v[36:51]
	v_add_f32_e32 v144, v68, v69
	ds_read_b128 v[140:143], v156 offset:4096
	ds_read_b64_tr_b16 v[100:101], v157 offset:49152
	ds_read_b64_tr_b16 v[102:103], v157 offset:49664
	v_add_f32_e32 v144, v70, v144
	v_add_f32_e32 v144, v71, v144
	v_add_f32_e32 v144, v72, v144
	v_add_f32_e32 v144, v73, v144
	v_cvt_pk_bf16_f32 v68, v68, v69
	v_cvt_pk_bf16_f32 v69, v70, v71
	v_mfma_f32_32x32x16_bf16 v[36:51], v[104:107], v[136:139], v[36:51]
	ds_read_b128 v[136:139], v156 offset:4608
	ds_read_b64_tr_b16 v[104:105], v157 offset:53248
	ds_read_b64_tr_b16 v[106:107], v157 offset:53760
	v_add_f32_e32 v70, v74, v144
	v_add_f32_e32 v70, v75, v70
	v_add_f32_e32 v70, v76, v70
	v_add_f32_e32 v148, v77, v70
	v_cvt_pk_bf16_f32 v70, v72, v73
	v_cvt_pk_bf16_f32 v71, v74, v75
	v_mfma_f32_32x32x16_bf16 v[84:99], v[108:111], v[132:135], v[84:99]
	ds_read_b128 v[144:147], v156 offset:6144
	ds_read_b64_tr_b16 v[108:109], v157 offset:50176
	ds_read_b64_tr_b16 v[110:111], v157 offset:50688
	v_add_f32_e32 v72, v78, v148
	v_add_f32_e32 v72, v79, v72
	v_add_f32_e32 v72, v80, v72
	v_add_f32_e32 v152, v81, v72
	v_cvt_pk_bf16_f32 v72, v76, v77
	v_cvt_pk_bf16_f32 v73, v78, v79
	v_mfma_f32_32x32x16_bf16 v[36:51], v[112:115], v[132:135], v[36:51]
	ds_read_b128 v[148:151], v156 offset:6656
	ds_read_b64_tr_b16 v[76:77], v157 offset:54272
	ds_read_b64_tr_b16 v[78:79], v157 offset:54784
	v_add_f32_e32 v74, v82, v152
	v_add_f32_e32 v74, v83, v74
	v_add_f32_e32 v74, v52, v74
	v_add_f32_e32 v132, v53, v74
	v_cvt_pk_bf16_f32 v74, v80, v81
	v_cvt_pk_bf16_f32 v75, v82, v83
	v_exp_f32_e32 v60, v60
	v_exp_f32_e32 v61, v61
	v_exp_f32_e32 v62, v62
	v_exp_f32_e32 v63, v63
	s_waitcnt lgkmcnt(0)
	v_mfma_f32_32x32x16_bf16 v[84:99], v[140:143], v[128:131], v[84:99]
	ds_read_b128 v[140:143], v156 offset:8192
	ds_read_b64_tr_b16 v[112:113], v157 offset:51200
	ds_read_b64_tr_b16 v[114:115], v157 offset:51712
	v_add_f32_e32 v80, v54, v132
	v_add_f32_e32 v80, v55, v80
	v_add_f32_e32 v80, v56, v80
	v_add_f32_e32 v132, v57, v80
	v_cvt_pk_bf16_f32 v80, v52, v53
	v_cvt_pk_bf16_f32 v81, v54, v55
	v_exp_f32_e32 v64, v64
	v_exp_f32_e32 v65, v65
	v_exp_f32_e32 v66, v66
	v_exp_f32_e32 v67, v67
	v_mfma_f32_32x32x16_bf16 v[36:51], v[136:139], v[128:131], v[36:51]
	ds_read_b128 v[152:155], v156 offset:8704
	ds_read_b64_tr_b16 v[128:129], v157 offset:55296
	ds_read_b64_tr_b16 v[130:131], v157 offset:55808
	v_add_f32_e32 v52, v58, v132
	v_add_f32_e32 v52, v59, v52
	v_add_f32_e32 v52, v60, v52
	v_add_f32_e32 v52, v61, v52
	v_cvt_pk_bf16_f32 v82, v56, v57
	v_cvt_pk_bf16_f32 v83, v58, v59
	v_mfma_f32_32x32x16_bf16 v[84:99], v[144:147], v[124:127], v[84:99]
	ds_read_b128 v[54:57], v156 offset:10240
	ds_read_b64_tr_b16 v[136:137], v157 offset:52224
	ds_read_b64_tr_b16 v[138:139], v157 offset:52736
	v_add_f32_e32 v52, v62, v52
	v_add_f32_e32 v52, v63, v52
	v_add_f32_e32 v52, v64, v52
	v_add_f32_e32 v52, v65, v52
	v_cvt_pk_bf16_f32 v132, v60, v61
	v_cvt_pk_bf16_f32 v133, v62, v63
	v_mfma_f32_32x32x16_bf16 v[36:51], v[148:151], v[124:127], v[36:51]
	ds_read_b128 v[58:61], v156 offset:10752
	ds_read_b64_tr_b16 v[124:125], v157 offset:56320
	ds_read_b64_tr_b16 v[126:127], v157 offset:56832
	v_add_f32_e32 v52, v66, v52
	v_add_f32_e32 v52, v67, v52
	v_cvt_pk_bf16_f32 v134, v64, v65
	v_cvt_pk_bf16_f32 v135, v66, v67
	s_waitcnt lgkmcnt(0)
	v_mfma_f32_32x32x16_bf16 v[84:99], v[140:143], v[120:123], v[84:99]
	v_mfma_f32_32x32x16_bf16 v[36:51], v[152:155], v[120:123], v[36:51]
	v_mfma_f32_32x32x16_bf16 v[84:99], v[54:57], v[116:119], v[84:99]
	v_mfma_f32_32x32x16_bf16 v[36:51], v[58:61], v[116:119], v[36:51]
	s_setprio 0
	s_cmp_lt_i32 s12, s52
	s_cbranch_scc0 .LBB0_1195
